# x1 pre-pass: U state tile via swapped MFMA operands + permlane32 swap, 16-byte stores instead of 2-byte stores
# baseline (speedup 1.0000x reference)
; __device__ __forceinline__ int crow(int r, int hi) { return (r & 3) + 8 * (r >> 2) + 4 * hi; }
; __device__ __forceinline__ int crow(int r, int hi) { return (r & 3) + 8 * (r >> 2) + 4 * hi; }
; #define MF32(a, b, c) __builtin_amdgcn_mfma_f32_32x32x16_f16(__builtin_bit_cast(h16x8, (a)), __builtin_bit_cast(h16x8, (b)), (c), 0, 0, 0)
; __device__ __forceinline__ void x1_wave(int item, int b0, const h16* __restrict__ proj, const float* __restrict__ small, const float* __restrict__ convw, ...
;     ...
;     const int lb = ((lane >> 4) & 1) * 32 + (lane & 3) * 8 + (4 * hi + ((lane & 15) >> 2)) * 64;
;     h16* up = U + ((size_t)lbh * 32 + c) * 8192;
; #pragma unroll 1
;     for (int vb = 0; vb < 4; ++vb) {
;         f32x16 a0 = f32x16{}, a1 = f32x16{};
; #pragma unroll
;         for (int ks = 0; ks < 4; ++ks) { const s16x8 vf = trfrag((lds_cptr)(R + W_V), vb, ks, lb);
;             a0 = MF32(vf, trfrag((lds_cptr)(R + W_K), 0, ks, lb), a0); a1 = MF32(vf, trfrag((lds_cptr)(R + W_K), 1, ks, lb), a1); }
; #pragma unroll
;         for (int r = 0; r < 16; ++r) { up[(vb * 32 + crow(r, hi)) * 64 + r32] = (h16)a0[r]; up[(vb * 32 + crow(r, hi)) * 64 + 32 + r32] = (h16)a1[r]; }
;     }
.LBB0_916:
	s_or_b64 exec, exec, s[0:1]
	s_lshl_b32 s0, s20, 2
	s_or_b32 s0, s0, s13
	s_ashr_i32 s1, s0, 31
	v_lshlrev_b32_e32 v0, 1, v174
	v_lshlrev_b32_e32 v1, 4, v178
	s_lshl_b64 s[0:1], s[0:1], 19
	v_readlane_b32 s15, v254, 28
	v_ashrrev_i32_e32 v33, 5, v174
	v_and_b32_e32 v0, 32, v0
	v_and_b32_e32 v1, 0xc0, v1
	s_add_u32 s0, s15, s0
	v_readlane_b32 s15, v254, 29
	s_waitcnt lgkmcnt(0)
	v_lshlrev_b32_e32 v34, 8, v33
	v_or3_b32 v0, v0, v1, v179
	s_addc_u32 s1, s15, s1
	s_lshl_b32 s15, s12, 14
	v_and_b32_e32 v32, 31, v174
	v_or_b32_e32 v1, v0, v34
	s_add_u32 s0, s0, s15
	s_mov_b32 s13, 4
	s_addc_u32 s1, s1, 0
	v_add_u32_e32 v35, s10, v0
	v_add_u32_e32 v36, s10, v1
	v_lshlrev_b32_e32 v37, 6, v32
	v_lshl_add_u32 v37, v33, 4, v37
.LBB0_917:
	v_add_u32_e32 v46, v35, v34
	ds_read_b64_tr_b16 v[16:17], v46
	ds_read_b64_tr_b16 v[18:19], v46 offset:512
	ds_read_b64_tr_b16 v[0:1], v36 offset:16384
	ds_read_b64_tr_b16 v[2:3], v36 offset:16896
	ds_read_b64_tr_b16 v[20:21], v36 offset:20480
	ds_read_b64_tr_b16 v[22:23], v36 offset:20992
	ds_read_b64_tr_b16 v[38:39], v46 offset:1024
	ds_read_b64_tr_b16 v[40:41], v46 offset:1536
	ds_read_b64_tr_b16 v[42:43], v36 offset:17408
	ds_read_b64_tr_b16 v[44:45], v36 offset:17920
	s_add_i32 s13, s13, -1
	v_add_u32_e32 v35, 0x1000, v35
	s_waitcnt lgkmcnt(6)
	v_mfma_f32_32x32x16_f16 v[0:15], v[0:3], v[16:19], 0
	s_cmp_lg_u32 s13, 0
	s_waitcnt lgkmcnt(4)
	v_mfma_f32_32x32x16_f16 v[16:31], v[20:23], v[16:19], 0
	s_waitcnt lgkmcnt(0)
	v_mfma_f32_32x32x16_f16 v[0:15], v[42:45], v[38:41], v[0:15]
	ds_read_b64_tr_b16 v[42:43], v36 offset:21504
	ds_read_b64_tr_b16 v[44:45], v36 offset:22016
	s_waitcnt lgkmcnt(0)
	v_mfma_f32_32x32x16_f16 v[16:31], v[42:45], v[38:41], v[16:31]
	ds_read_b64_tr_b16 v[38:39], v46 offset:2048
	ds_read_b64_tr_b16 v[40:41], v46 offset:2560
	ds_read_b64_tr_b16 v[42:43], v36 offset:18432
	ds_read_b64_tr_b16 v[44:45], v36 offset:18944
	s_waitcnt lgkmcnt(0)
	v_mfma_f32_32x32x16_f16 v[0:15], v[42:45], v[38:41], v[0:15]
	ds_read_b64_tr_b16 v[42:43], v36 offset:22528
	ds_read_b64_tr_b16 v[44:45], v36 offset:23040
	s_waitcnt lgkmcnt(0)
	v_mfma_f32_32x32x16_f16 v[16:31], v[42:45], v[38:41], v[16:31]
	ds_read_b64_tr_b16 v[38:39], v46 offset:3072
	ds_read_b64_tr_b16 v[40:41], v46 offset:3584
	ds_read_b64_tr_b16 v[42:43], v36 offset:19456
	ds_read_b64_tr_b16 v[44:45], v36 offset:19968
	s_waitcnt lgkmcnt(0)
	v_mfma_f32_32x32x16_f16 v[0:15], v[42:45], v[38:41], v[0:15]
	ds_read_b64_tr_b16 v[42:43], v36 offset:23552
	ds_read_b64_tr_b16 v[44:45], v36 offset:24064
	s_waitcnt lgkmcnt(0)
	v_mfma_f32_32x32x16_f16 v[16:31], v[42:45], v[38:41], v[16:31]
	s_nop 7
	s_nop 7
	v_cvt_pk_f16_f32 v0, v0, v1
	v_cvt_pk_f16_f32 v1, v2, v3
	v_cvt_pk_f16_f32 v2, v8, v9
	v_cvt_pk_f16_f32 v3, v10, v11
	v_cvt_pk_f16_f32 v4, v4, v5
	v_cvt_pk_f16_f32 v5, v6, v7
	v_cvt_pk_f16_f32 v6, v12, v13
	v_cvt_pk_f16_f32 v7, v14, v15
	v_cvt_pk_f16_f32 v16, v16, v17
	v_cvt_pk_f16_f32 v17, v18, v19
	v_cvt_pk_f16_f32 v18, v24, v25
	v_cvt_pk_f16_f32 v19, v26, v27
	v_cvt_pk_f16_f32 v20, v20, v21
	v_cvt_pk_f16_f32 v21, v22, v23
	v_cvt_pk_f16_f32 v22, v28, v29
	v_cvt_pk_f16_f32 v23, v30, v31
	v_ashrrev_i32_e32 v39, 31, v37
	v_mov_b32_e32 v38, v37
	v_permlane32_swap_b32_e32 v0, v2
	v_permlane32_swap_b32_e32 v1, v3
	v_permlane32_swap_b32_e32 v4, v6
	v_permlane32_swap_b32_e32 v5, v7
	v_permlane32_swap_b32_e32 v16, v18
	v_permlane32_swap_b32_e32 v17, v19
	v_permlane32_swap_b32_e32 v20, v22
	v_permlane32_swap_b32_e32 v21, v23
	v_lshl_add_u64 v[38:39], v[38:39], 1, s[0:1]
	v_add_u32_e32 v37, 0x800, v37
	s_nop 1
	global_store_dwordx4 v[38:39], v[0:3], off
	global_store_dwordx4 v[38:39], v[4:7], off offset:16
	global_store_dwordx4 v[38:39], v[16:19], off offset:64
	global_store_dwordx4 v[38:39], v[20:23], off offset:80
	s_cbranch_scc1 .LBB0_917
	v_lshlrev_b32_e32 v0, 1, v32
	v_lshl_or_b32 v0, v33, 12, v0
	v_add_u32_e32 v0, s11, v0
	v_mov_b32_e32 v1, 0
	s_mov_b32 s0, 0
